# P2 attention: QK^T and PV LDS fragment reads issued in a ring ahead of the MFMAs (counted lgkmcnt)
# speedup vs baseline: 1.0060x; 1.0060x over previous
.LBB0_243:
	s_mul_hi_i32 s56, s55, 0x2aaaaaab
	s_lshr_b32 s57, s56, 31
	s_ashr_i32 s56, s56, 3
	s_mul_hi_i32 s60, s55, 0x38e38e39
	s_add_i32 s56, s56, s57
	s_lshr_b32 s61, s60, 31
	s_ashr_i32 s60, s60, 7
	s_mul_i32 s57, s56, 0xffffffd0
	s_add_i32 s64, s60, s61
	s_add_i32 s57, s55, s57
	s_mul_i32 s60, s64, -12
	s_ashr_i32 s58, s57, 4
	s_and_b32 s59, s55, 15
	s_add_i32 s56, s60, s56
	s_cmp_lt_u32 s57, 16
	s_cselect_b64 s[60:61], -1, 0
	s_cmp_eq_u32 s58, 1
	s_cselect_b64 s[62:63], -1, 0
	s_bfe_u32 s57, s55, 0x20002
	s_and_b64 s[66:67], s[62:63], exec
	s_cselect_b32 s57, s57, s59
	s_and_b64 s[66:67], s[60:61], exec
	s_cselect_b32 s57, 0, s57
	s_and_b32 s65, s55, 3
	s_and_b64 s[66:67], s[62:63], exec
	s_cselect_b32 s65, s65, 0
	s_and_b64 s[66:67], s[60:61], exec
	s_cselect_b32 s59, s59, s65
	s_ashr_i32 s65, s64, 31
	s_lshl_b64 s[64:65], s[64:65], 11
	s_or_b32 s66, s64, s57
	s_lshl_b32 s80, s59, 7
	s_mul_i32 s67, s66, 0x2800
	s_mul_hi_u32 s66, s66, 0x2800
	s_mul_i32 s68, s65, 0x2800
	s_add_i32 s82, s80, 0xffffff80
	s_add_i32 s66, s66, s68
	s_add_u32 s68, s3, s67
	s_addc_u32 s69, s33, s66
	s_lshl_b32 s66, s56, 7
	s_ashr_i32 s67, s66, 31
	s_lshl_b64 s[66:67], s[66:67], 1
	s_add_u32 s68, s68, s66
	s_addc_u32 s69, s69, s67
	s_and_b64 s[70:71], s[62:63], exec
	s_movk_i32 s70, 0x5000
	s_cselect_b32 s81, s70, 0x14000
	s_and_b64 s[70:71], s[60:61], exec
	s_cselect_b32 s83, 0x1400, s81
	v_add_u32_e32 v50, s80, v58
	v_mad_u64_u32 v[120:121], s[70:71], s83, v50, 0
	s_and_b64 s[70:71], s[62:63], exec
	s_movk_i32 s70, 0x7f
	s_cselect_b32 s80, 0x1ff, s70
	s_and_b64 s[70:71], s[60:61], exec
	s_cselect_b32 s84, 0x7ff, s80
	v_or_b32_e32 v2, s82, v59
	s_cmp_eq_u32 s59, 0
	v_or_b32_e32 v10, s82, v60
	s_cselect_b64 s[70:71], -1, 0
	v_min_i32_e32 v2, s84, v2
	v_min_i32_e32 v10, s84, v10
	v_mov_b32_e32 v53, v51
	v_cndmask_b32_e64 v2, v2, 0, s[70:71]
	v_cndmask_b32_e64 v10, v10, 0, s[70:71]
	v_lshl_add_u64 v[112:113], s[68:69], 0, v[52:53]
	v_mad_u64_u32 v[2:3], s[80:81], s83, v2, 0
	v_mad_u64_u32 v[10:11], s[80:81], s83, v10, 0
	v_lshl_add_u64 v[6:7], v[2:3], 1, v[112:113]
	v_lshl_add_u64 v[14:15], v[10:11], 1, v[112:113]
	v_or_b32_e32 v18, s82, v61
	global_load_dwordx4 v[2:5], v[6:7], off offset:3072
	global_load_dwordx4 v[10:13], v[14:15], off offset:3072
	v_add_co_u32_e32 v6, vcc, s44, v6
	v_min_i32_e32 v18, s84, v18
	v_add_u32_e32 v34, s82, v63
	v_addc_co_u32_e32 v7, vcc, 0, v7, vcc
	v_cndmask_b32_e64 v18, v18, 0, s[70:71]
	v_min_i32_e32 v34, s84, v34
	v_add_co_u32_e32 v14, vcc, s44, v14
	v_mad_u64_u32 v[18:19], s[70:71], s83, v18, 0
	v_mad_u64_u32 v[34:35], s[70:71], s83, v34, 0
	v_addc_co_u32_e32 v15, vcc, 0, v15, vcc
	v_lshl_add_u64 v[22:23], v[18:19], 1, v[112:113]
	v_lshl_add_u64 v[38:39], v[34:35], 1, v[112:113]
	global_load_dwordx4 v[18:21], v[22:23], off offset:3072
	global_load_dwordx4 v[34:37], v[38:39], off offset:3072
	v_add_co_u32_e32 v22, vcc, s44, v22
	v_or_b32_e32 v26, s82, v62
	s_nop 0
	v_addc_co_u32_e32 v23, vcc, 0, v23, vcc
	global_load_dwordx4 v[6:9], v[6:7], off offset:2048
	v_min_i32_e32 v27, s84, v26
	v_cmp_lt_i32_e32 vcc, -1, v26
	v_add_u32_e32 v42, s82, v64
	v_min_i32_e32 v42, s84, v42
	v_cndmask_b32_e32 v26, 0, v27, vcc
	global_load_dwordx4 v[14:17], v[14:15], off offset:2048
	v_mad_u64_u32 v[26:27], s[70:71], s83, v26, 0
	v_mad_u64_u32 v[42:43], s[70:71], s83, v42, 0
	v_lshl_add_u64 v[30:31], v[26:27], 1, v[112:113]
	v_lshl_add_u64 v[46:47], v[42:43], 1, v[112:113]
	global_load_dwordx4 v[22:25], v[22:23], off offset:2048
	v_add_u32_e32 v53, s82, v65
	global_load_dwordx4 v[26:29], v[30:31], off offset:3072
	global_load_dwordx4 v[42:45], v[46:47], off offset:3072
	v_add_co_u32_e32 v30, vcc, s44, v30
	v_min_i32_e32 v53, s84, v53
	s_nop 0
	v_addc_co_u32_e32 v31, vcc, 0, v31, vcc
	global_load_dwordx4 v[30:33], v[30:31], off offset:2048
	v_add_co_u32_e32 v38, vcc, s44, v38
	v_mad_u64_u32 v[104:105], s[70:71], s83, v53, 0
	v_add_u32_e32 v53, s82, v66
	v_addc_co_u32_e32 v39, vcc, 0, v39, vcc
	v_min_i32_e32 v53, s84, v53
	global_load_dwordx4 v[38:41], v[38:39], off offset:2048
	v_add_co_u32_e32 v46, vcc, s44, v46
	v_mad_u64_u32 v[114:115], s[70:71], s83, v53, 0
	s_nop 0
	v_addc_co_u32_e32 v47, vcc, 0, v47, vcc
	v_lshl_add_u64 v[108:109], v[104:105], 1, v[112:113]
	v_lshl_add_u64 v[116:117], v[114:115], 1, v[112:113]
	global_load_dwordx4 v[46:49], v[46:47], off offset:2048
	v_mov_b32_e32 v55, v51
	global_load_dwordx4 v[104:107], v[108:109], off offset:3072
	global_load_dwordx4 v[112:115], v[116:117], off offset:3072
	v_add_co_u32_e32 v108, vcc, s44, v108
	s_cmp_lg_u32 s59, 0
	s_nop 0
	v_addc_co_u32_e32 v109, vcc, 0, v109, vcc
	global_load_dwordx4 v[108:111], v[108:109], off offset:2048
	v_add_co_u32_e32 v116, vcc, s44, v116
	s_mov_b32 s59, 0xff800000
	s_nop 0
	v_addc_co_u32_e32 v117, vcc, 0, v117, vcc
	global_load_dwordx4 v[116:119], v[116:117], off offset:2048
	s_waitcnt vmcnt(15)
	ds_write_b128 v80, v[2:5]
	s_waitcnt vmcnt(11)
	ds_write_b128 v81, v[6:9]
	ds_write_b128 v82, v[10:13]
	s_waitcnt vmcnt(10)
	ds_write_b128 v83, v[14:17]
	ds_write_b128 v84, v[18:21]
	s_waitcnt vmcnt(9)
	ds_write_b128 v85, v[22:25]
	s_waitcnt vmcnt(8)
	ds_write_b128 v86, v[26:29]
	s_waitcnt vmcnt(6)
	ds_write_b128 v87, v[30:33]
	ds_write_b128 v88, v[34:37]
	s_waitcnt vmcnt(5)
	ds_write_b128 v89, v[38:41]
	ds_write_b128 v90, v[42:45]
	s_waitcnt vmcnt(4)
	ds_write_b128 v91, v[46:49]
	s_waitcnt vmcnt(3)
	ds_write_b128 v92, v[104:107]
	s_waitcnt vmcnt(1)
	ds_write_b128 v93, v[108:111]
	ds_write_b128 v94, v[112:115]
	s_waitcnt vmcnt(0)
	ds_write_b128 v95, v[116:119]
	v_lshl_add_u64 v[2:3], v[120:121], 1, s[68:69]
	s_waitcnt lgkmcnt(0)
	s_barrier
	v_lshl_add_u64 v[2:3], v[2:3], 0, v[54:55]
	global_load_dwordx4 v[46:49], v[2:3], off
	global_load_dwordx4 v[42:45], v[2:3], off offset:64
	global_load_dwordx4 v[38:41], v[2:3], off offset:128
	global_load_dwordx4 v[6:9], v[2:3], off offset:192
	s_cselect_b64 s[68:69], -1, 0
	s_or_b64 s[70:71], s[68:69], s[26:27]
	s_and_b64 vcc, s[70:71], s[6:7]
	ds_read_b128 v[132:135], v96
	ds_read_b128 v[136:139], v97
	ds_read_b128 v[152:155], v98
	ds_read_b128 v[168:171], v99
	ds_read_b128 v[172:175], v96 offset:4096
	ds_read_b128 v[176:179], v97 offset:4096
	ds_read_b128 v[180:183], v98 offset:4096
	ds_read_b128 v[192:195], v99 offset:4096
	ds_read_b128 v[196:199], v96 offset:8192
	ds_read_b128 v[200:203], v97 offset:8192
	ds_read_b128 v[204:207], v98 offset:8192
	ds_read_b128 v[208:211], v99 offset:8192
	ds_read_b128 v[212:215], v96 offset:12288
	ds_read_b128 v[216:219], v97 offset:12288
	ds_read_b128 v[220:223], v98 offset:12288
	s_waitcnt vmcnt(3) lgkmcnt(14)
	v_mfma_f32_16x16x32_bf16 v[2:5], v[132:135], v[46:49], 0
	ds_read_b128 v[228:231], v99 offset:12288
	s_waitcnt vmcnt(2) lgkmcnt(14)
	v_mfma_f32_16x16x32_bf16 v[2:5], v[136:139], v[42:45], v[2:5]
	ds_read_b128 v[132:135], v96 offset:16384
	s_waitcnt vmcnt(1) lgkmcnt(14)
	v_mfma_f32_16x16x32_bf16 v[2:5], v[152:155], v[38:41], v[2:5]
	ds_read_b128 v[136:139], v97 offset:16384
	s_waitcnt vmcnt(0) lgkmcnt(14)
	v_mfma_f32_16x16x32_bf16 v[2:5], v[168:171], v[6:9], v[2:5]
	ds_read_b128 v[152:155], v98 offset:16384
	s_waitcnt lgkmcnt(14)
	v_mfma_f32_16x16x32_bf16 v[10:13], v[172:175], v[46:49], 0
	ds_read_b128 v[168:171], v99 offset:16384
	s_waitcnt lgkmcnt(14)
	v_mfma_f32_16x16x32_bf16 v[10:13], v[176:179], v[42:45], v[10:13]
	ds_read_b128 v[172:175], v96 offset:20480
	s_waitcnt lgkmcnt(14)
	v_mfma_f32_16x16x32_bf16 v[10:13], v[180:183], v[38:41], v[10:13]
	ds_read_b128 v[176:179], v97 offset:20480
	s_waitcnt lgkmcnt(14)
	v_mfma_f32_16x16x32_bf16 v[10:13], v[192:195], v[6:9], v[10:13]
	ds_read_b128 v[180:183], v98 offset:20480
	s_waitcnt lgkmcnt(14)
	v_mfma_f32_16x16x32_bf16 v[14:17], v[196:199], v[46:49], 0
	ds_read_b128 v[192:195], v99 offset:20480
	s_waitcnt lgkmcnt(14)
	v_mfma_f32_16x16x32_bf16 v[14:17], v[200:203], v[42:45], v[14:17]
	ds_read_b128 v[196:199], v96 offset:24576
	s_waitcnt lgkmcnt(14)
	v_mfma_f32_16x16x32_bf16 v[14:17], v[204:207], v[38:41], v[14:17]
	ds_read_b128 v[200:203], v97 offset:24576
	s_waitcnt lgkmcnt(14)
	v_mfma_f32_16x16x32_bf16 v[14:17], v[208:211], v[6:9], v[14:17]
	ds_read_b128 v[204:207], v98 offset:24576
	s_waitcnt lgkmcnt(14)
	v_mfma_f32_16x16x32_bf16 v[18:21], v[212:215], v[46:49], 0
	ds_read_b128 v[208:211], v99 offset:24576
	s_waitcnt lgkmcnt(14)
	v_mfma_f32_16x16x32_bf16 v[18:21], v[216:219], v[42:45], v[18:21]
	ds_read_b128 v[212:215], v96 offset:28672
	s_waitcnt lgkmcnt(14)
	v_mfma_f32_16x16x32_bf16 v[18:21], v[220:223], v[38:41], v[18:21]
	ds_read_b128 v[216:219], v97 offset:28672
	s_waitcnt lgkmcnt(14)
	v_mfma_f32_16x16x32_bf16 v[18:21], v[228:231], v[6:9], v[18:21]
	ds_read_b128 v[220:223], v98 offset:28672
	s_waitcnt lgkmcnt(14)
	v_mfma_f32_16x16x32_bf16 v[22:25], v[132:135], v[46:49], 0
	ds_read_b128 v[228:231], v99 offset:28672
	s_waitcnt lgkmcnt(14)
	v_mfma_f32_16x16x32_bf16 v[22:25], v[136:139], v[42:45], v[22:25]
	ds_read_b128 v[132:135], v96 offset:32768
	s_waitcnt lgkmcnt(14)
	v_mfma_f32_16x16x32_bf16 v[22:25], v[152:155], v[38:41], v[22:25]
	ds_read_b128 v[136:139], v97 offset:32768
	s_waitcnt lgkmcnt(14)
	v_mfma_f32_16x16x32_bf16 v[22:25], v[168:171], v[6:9], v[22:25]
	ds_read_b128 v[152:155], v98 offset:32768
	s_waitcnt lgkmcnt(14)
	v_mfma_f32_16x16x32_bf16 v[26:29], v[172:175], v[46:49], 0
	ds_read_b128 v[168:171], v99 offset:32768
	s_waitcnt lgkmcnt(14)
	v_mfma_f32_16x16x32_bf16 v[26:29], v[176:179], v[42:45], v[26:29]
	s_waitcnt lgkmcnt(13)
	v_mfma_f32_16x16x32_bf16 v[26:29], v[180:183], v[38:41], v[26:29]
	s_waitcnt lgkmcnt(12)
	v_mfma_f32_16x16x32_bf16 v[26:29], v[192:195], v[6:9], v[26:29]
	s_waitcnt lgkmcnt(11)
	v_mfma_f32_16x16x32_bf16 v[30:33], v[196:199], v[46:49], 0
	s_waitcnt lgkmcnt(10)
	v_mfma_f32_16x16x32_bf16 v[30:33], v[200:203], v[42:45], v[30:33]
	s_waitcnt lgkmcnt(9)
	v_mfma_f32_16x16x32_bf16 v[30:33], v[204:207], v[38:41], v[30:33]
	s_waitcnt lgkmcnt(8)
	v_mfma_f32_16x16x32_bf16 v[30:33], v[208:211], v[6:9], v[30:33]
	s_waitcnt lgkmcnt(7)
	v_mfma_f32_16x16x32_bf16 v[34:37], v[212:215], v[46:49], 0
	s_waitcnt lgkmcnt(6)
	v_mfma_f32_16x16x32_bf16 v[34:37], v[216:219], v[42:45], v[34:37]
	s_waitcnt lgkmcnt(5)
	v_mfma_f32_16x16x32_bf16 v[34:37], v[220:223], v[38:41], v[34:37]
	s_waitcnt lgkmcnt(4)
	v_mfma_f32_16x16x32_bf16 v[34:37], v[228:231], v[6:9], v[34:37]
	s_waitcnt lgkmcnt(3)
	v_mfma_f32_16x16x32_bf16 v[104:107], v[132:135], v[46:49], 0
	s_waitcnt lgkmcnt(2)
	v_mfma_f32_16x16x32_bf16 v[104:107], v[136:139], v[42:45], v[104:107]
	s_waitcnt lgkmcnt(1)
	v_mfma_f32_16x16x32_bf16 v[104:107], v[152:155], v[38:41], v[104:107]
	s_waitcnt lgkmcnt(0)
	v_mfma_f32_16x16x32_bf16 v[6:9], v[168:171], v[6:9], v[104:107]
	s_nop 2
	v_cndmask_b32_e32 v38, v101, v2, vcc
	s_and_b64 vcc, s[70:71], s[8:9]
	v_cndmask_b32_e32 v39, v101, v3, vcc
	s_and_b64 vcc, s[70:71], s[10:11]
	v_cndmask_b32_e32 v4, v101, v4, vcc
	s_and_b64 vcc, s[70:71], s[12:13]
	v_max3_f32 v2, v38, s59, v39
	v_cndmask_b32_e32 v5, v101, v5, vcc
	s_or_b64 vcc, s[28:29], s[68:69]
	v_max3_f32 v2, v2, v4, v5
	v_cndmask_b32_e32 v10, v101, v10, vcc
	v_cndmask_b32_e32 v11, v101, v11, vcc
	v_max3_f32 v2, v2, v10, v11
	v_cndmask_b32_e32 v12, v101, v12, vcc
	v_cndmask_b32_e32 v13, v101, v13, vcc
	s_or_b64 vcc, s[30:31], s[68:69]
	v_max3_f32 v2, v2, v12, v13
	v_cndmask_b32_e32 v14, v101, v14, vcc
	v_cndmask_b32_e32 v15, v101, v15, vcc
	v_max3_f32 v2, v2, v14, v15
	v_cndmask_b32_e32 v16, v101, v16, vcc
	v_cndmask_b32_e32 v17, v101, v17, vcc
	s_or_b64 vcc, s[34:35], s[68:69]
	v_max3_f32 v2, v2, v16, v17
	v_cndmask_b32_e32 v40, v101, v18, vcc
	v_cndmask_b32_e32 v41, v101, v19, vcc
	v_max3_f32 v2, v2, v40, v41
	v_cndmask_b32_e32 v20, v101, v20, vcc
	v_cndmask_b32_e32 v21, v101, v21, vcc
	s_or_b64 vcc, s[36:37], s[68:69]
	v_max3_f32 v2, v2, v20, v21
	v_cndmask_b32_e32 v22, v101, v22, vcc
	v_cndmask_b32_e32 v23, v101, v23, vcc
	v_max3_f32 v2, v2, v22, v23
	v_cndmask_b32_e32 v24, v101, v24, vcc
	v_cndmask_b32_e32 v42, v101, v25, vcc
	s_or_b64 vcc, s[38:39], s[68:69]
	v_max3_f32 v2, v2, v24, v42
	v_cndmask_b32_e32 v43, v101, v26, vcc
	v_cndmask_b32_e32 v44, v101, v27, vcc
	v_max3_f32 v2, v2, v43, v44
	v_cndmask_b32_e32 v45, v101, v28, vcc
	v_cndmask_b32_e32 v46, v101, v29, vcc
	s_or_b64 vcc, s[40:41], s[68:69]
	v_max3_f32 v2, v2, v45, v46
	v_cndmask_b32_e32 v47, v101, v30, vcc
	v_cndmask_b32_e32 v48, v101, v31, vcc
	v_max3_f32 v2, v2, v47, v48
	v_cndmask_b32_e32 v49, v101, v32, vcc
	v_cndmask_b32_e32 v53, v101, v33, vcc
	s_or_b64 vcc, s[42:43], s[68:69]
	v_max3_f32 v2, v2, v49, v53
	v_cndmask_b32_e32 v55, v101, v34, vcc
	v_cndmask_b32_e32 v57, v101, v35, vcc
	v_max3_f32 v2, v2, v55, v57
	v_cndmask_b32_e32 v103, v101, v36, vcc
	v_cndmask_b32_e32 v104, v101, v37, vcc
	v_max3_f32 v2, v2, v103, v104
	v_cndmask_b32_e64 v6, v101, v6, s[14:15]
	v_cndmask_b32_e64 v7, v101, v7, s[16:17]
	v_and_b32_e32 v18, 64, v100
	v_max3_f32 v3, v2, v6, v7
	v_cndmask_b32_e64 v2, v101, v9, s[20:21]
	v_xor_b32_e32 v9, 16, v100
	v_add_u32_e32 v18, 64, v18
	v_cmp_lt_i32_e32 vcc, v9, v18
	v_cndmask_b32_e64 v8, v101, v8, s[18:19]
	v_max3_f32 v3, v3, v8, v2
	v_cndmask_b32_e32 v9, v100, v9, vcc
	v_lshlrev_b32_e32 v105, 2, v9
	ds_bpermute_b32 v9, v105, v3
	s_and_b64 s[62:63], s[62:63], exec
	s_cselect_b32 s59, 2, 4
	s_and_b64 s[60:61], s[60:61], exec
	s_cselect_b32 s59, 0, s59
	s_waitcnt lgkmcnt(0)
	v_max_f32_e32 v9, v9, v9
	v_max_f32_e32 v3, v3, v9
	v_xor_b32_e32 v9, 32, v100
	v_cmp_lt_i32_e32 vcc, v9, v18
	s_nop 1
	v_cndmask_b32_e32 v9, v100, v9, vcc
	v_lshlrev_b32_e32 v106, 2, v9
	ds_bpermute_b32 v9, v106, v3
	s_waitcnt lgkmcnt(0)
	v_max_f32_e32 v9, v9, v9
	v_max_f32_e32 v3, v3, v9
	v_pk_mul_f32 v[18:19], v[2:3], s[54:55] op_sel_hi:[1,0]
	s_nop 0
	v_fma_f32 v4, v4, s54, -v19
	v_exp_f32_e32 v109, v4
	v_fma_f32 v4, v5, s54, -v19
	v_exp_f32_e32 v110, v4
	v_fma_f32 v4, v10, s54, -v19
	v_exp_f32_e32 v111, v4
	v_fma_f32 v4, v11, s54, -v19
	v_exp_f32_e32 v112, v4
	v_fma_f32 v4, v12, s54, -v19
	v_fma_f32 v2, v38, s54, -v19
	v_exp_f32_e32 v113, v4
	v_fma_f32 v4, v13, s54, -v19
	v_exp_f32_e32 v107, v2
	v_fma_f32 v9, v39, s54, -v19
	v_exp_f32_e32 v114, v4
	v_fma_f32 v4, v14, s54, -v19
	v_exp_f32_e32 v108, v9
	v_exp_f32_e32 v33, v4
	v_fma_f32 v4, v15, s54, -v19
	v_exp_f32_e32 v34, v4
	v_fma_f32 v4, v16, s54, -v19
	v_exp_f32_e32 v35, v4
	v_fma_f32 v4, v17, s54, -v19
	v_add_f32_e32 v2, 0, v107
	v_exp_f32_e32 v36, v4
	v_fma_f32 v4, v40, s54, -v19
	v_add_f32_e32 v2, v108, v2
	v_exp_f32_e32 v37, v4
	v_fma_f32 v4, v41, s54, -v19
	v_add_f32_e32 v2, v109, v2
	v_exp_f32_e32 v38, v4
	v_fma_f32 v4, v20, s54, -v19
	v_add_f32_e32 v2, v110, v2
	v_exp_f32_e32 v39, v4
	v_fma_f32 v4, v21, s54, -v19
	v_add_f32_e32 v2, v111, v2
	v_exp_f32_e32 v40, v4
	v_fma_f32 v4, v22, s54, -v19
	v_add_f32_e32 v2, v112, v2
	v_exp_f32_e32 v25, v4
	v_fma_f32 v4, v23, s54, -v19
	v_add_f32_e32 v2, v113, v2
	v_exp_f32_e32 v26, v4
	v_fma_f32 v4, v24, s54, -v19
	v_add_f32_e32 v2, v114, v2
	v_exp_f32_e32 v27, v4
	v_fma_f32 v4, v42, s54, -v19
	v_add_f32_e32 v2, v33, v2
	v_exp_f32_e32 v28, v4
	v_fma_f32 v4, v43, s54, -v19
	v_add_f32_e32 v2, v34, v2
	v_exp_f32_e32 v29, v4
	v_fma_f32 v4, v44, s54, -v19
	v_add_f32_e32 v2, v35, v2
	v_exp_f32_e32 v30, v4
	v_fma_f32 v4, v45, s54, -v19
	v_add_f32_e32 v2, v36, v2
	v_exp_f32_e32 v31, v4
	v_fma_f32 v4, v46, s54, -v19
	v_add_f32_e32 v2, v37, v2
	v_exp_f32_e32 v32, v4
	v_fma_f32 v4, v47, s54, -v19
	v_add_f32_e32 v2, v38, v2
	v_exp_f32_e32 v9, v4
	v_fma_f32 v4, v48, s54, -v19
	v_add_f32_e32 v2, v39, v2
	v_exp_f32_e32 v10, v4
	v_fma_f32 v4, v49, s54, -v19
	v_add_f32_e32 v2, v40, v2
	v_exp_f32_e32 v11, v4
	v_fma_f32 v4, v53, s54, -v19
	v_add_f32_e32 v2, v25, v2
	v_exp_f32_e32 v12, v4
	v_fma_f32 v4, v55, s54, -v19
	v_add_f32_e32 v2, v26, v2
	v_exp_f32_e32 v13, v4
	v_fma_f32 v4, v57, s54, -v19
	v_add_f32_e32 v2, v27, v2
	v_exp_f32_e32 v14, v4
	v_fma_f32 v4, v103, s54, -v19
	v_add_f32_e32 v2, v28, v2
	v_exp_f32_e32 v15, v4
	v_fma_f32 v4, v104, s54, -v19
	v_add_f32_e32 v2, v29, v2
	v_exp_f32_e32 v16, v4
	v_fma_f32 v4, v6, s54, -v19
	v_add_f32_e32 v2, v30, v2
	v_exp_f32_e32 v5, v4
	v_fma_f32 v4, v7, s54, -v19
	v_add_f32_e32 v2, v31, v2
	v_exp_f32_e32 v6, v4
	v_fma_f32 v4, v8, s54, -v19
	v_add_f32_e32 v2, v32, v2
	v_exp_f32_e32 v7, v4
	v_sub_f32_e32 v4, v18, v19
	v_add_u32_e32 v124, v67, v69
	v_add_u32_e32 v125, v67, v70
	v_add_u32_e32 v126, v67, v71
	v_add_u32_e32 v127, v67, v72
	v_add_u32_e32 v128, v67, v73
	v_add_u32_e32 v129, v67, v74
	v_add_u32_e32 v130, v67, v75
	v_add_u32_e32 v131, v67, v76
	ds_read_b64_tr_b16 v[196:197], v124
	ds_read_b64_tr_b16 v[198:199], v124 offset:4096
	ds_read_b64_tr_b16 v[200:201], v125
	ds_read_b64_tr_b16 v[202:203], v125 offset:4096
	ds_read_b64_tr_b16 v[204:205], v126
	ds_read_b64_tr_b16 v[206:207], v126 offset:4096
	ds_read_b64_tr_b16 v[208:209], v127
	ds_read_b64_tr_b16 v[210:211], v127 offset:4096
	ds_read_b64_tr_b16 v[212:213], v128
	ds_read_b64_tr_b16 v[214:215], v128 offset:4096
	ds_read_b64_tr_b16 v[216:217], v129
	ds_read_b64_tr_b16 v[218:219], v129 offset:4096
	ds_read_b64_tr_b16 v[220:221], v130
	ds_read_b64_tr_b16 v[222:223], v130 offset:4096
	v_cvt_pk_bf16_f32 v42, v107, v108
	v_cvt_pk_bf16_f32 v43, v109, v110
	v_cvt_pk_bf16_f32 v44, v111, v112
	v_cvt_pk_bf16_f32 v45, v113, v114
	v_add_f32_e32 v2, v9, v2
	v_add_f32_e32 v2, v10, v2
	v_add_f32_e32 v2, v11, v2
	v_add_f32_e32 v2, v12, v2
	v_add_f32_e32 v2, v13, v2
	v_add_f32_e32 v2, v14, v2
	v_add_f32_e32 v2, v15, v2
	v_add_f32_e32 v2, v16, v2
	v_exp_f32_e32 v8, v4
	v_add_f32_e32 v2, v5, v2
	v_add_f32_e32 v2, v6, v2
	v_add_f32_e32 v2, v7, v2
	v_cvt_pk_bf16_f32 v34, v33, v34
	v_cvt_pk_bf16_f32 v35, v35, v36
	v_cvt_pk_bf16_f32 v36, v37, v38
	v_cvt_pk_bf16_f32 v37, v39, v40
	v_add_f32_e32 v2, v8, v2
	ds_bpermute_b32 v4, v105, v2
	v_cvt_pk_bf16_f32 v26, v25, v26
	v_cvt_pk_bf16_f32 v27, v27, v28
	v_cvt_pk_bf16_f32 v28, v29, v30
	v_cvt_pk_bf16_f32 v29, v31, v32
	v_cvt_pk_bf16_f32 v10, v9, v10
	v_cvt_pk_bf16_f32 v11, v11, v12
	v_cvt_pk_bf16_f32 v12, v13, v14
	v_cvt_pk_bf16_f32 v13, v15, v16
	s_waitcnt lgkmcnt(0)
	v_add_f32_e32 v2, v2, v4
	ds_bpermute_b32 v4, v106, v2
	v_cvt_pk_bf16_f32 v6, v5, v6
	v_cvt_pk_bf16_f32 v7, v7, v8
	v_mov_b32_e32 v8, v51
	v_mov_b32_e32 v9, v51
	v_mov_b32_e32 v57, v51
	s_waitcnt lgkmcnt(0)
	v_add_f32_e32 v2, v2, v4
	v_div_scale_f32 v4, s[68:69], v2, v2, 1.0
	v_rcp_f32_e32 v5, v4
	v_mfma_f32_16x16x32_bf16 v[132:135], v[196:199], v[42:45], 0
	ds_read_b64_tr_b16 v[228:229], v131
	ds_read_b64_tr_b16 v[230:231], v131 offset:4096
	v_mfma_f32_16x16x32_bf16 v[136:139], v[200:203], v[42:45], 0
	ds_read_b64_tr_b16 v[196:197], v124 offset:8192
	ds_read_b64_tr_b16 v[198:199], v124 offset:12288
	v_mfma_f32_16x16x32_bf16 v[152:155], v[204:207], v[42:45], 0
	ds_read_b64_tr_b16 v[200:201], v125 offset:8192
	ds_read_b64_tr_b16 v[202:203], v125 offset:12288
	v_mfma_f32_16x16x32_bf16 v[168:171], v[208:211], v[42:45], 0
	ds_read_b64_tr_b16 v[204:205], v126 offset:8192
	ds_read_b64_tr_b16 v[206:207], v126 offset:12288
	v_mfma_f32_16x16x32_bf16 v[172:175], v[212:215], v[42:45], 0
	ds_read_b64_tr_b16 v[208:209], v127 offset:8192
	ds_read_b64_tr_b16 v[210:211], v127 offset:12288
	v_mfma_f32_16x16x32_bf16 v[176:179], v[216:219], v[42:45], 0
	ds_read_b64_tr_b16 v[212:213], v128 offset:8192
	ds_read_b64_tr_b16 v[214:215], v128 offset:12288
	v_mfma_f32_16x16x32_bf16 v[180:183], v[220:223], v[42:45], 0
	ds_read_b64_tr_b16 v[216:217], v129 offset:8192
	ds_read_b64_tr_b16 v[218:219], v129 offset:12288
	s_waitcnt lgkmcnt(12)
	v_mfma_f32_16x16x32_bf16 v[192:195], v[228:231], v[42:45], 0
	ds_read_b64_tr_b16 v[220:221], v130 offset:8192
	ds_read_b64_tr_b16 v[222:223], v130 offset:12288
	s_waitcnt lgkmcnt(12)
	v_mfma_f32_16x16x32_bf16 v[132:135], v[196:199], v[34:37], v[132:135]
	ds_read_b64_tr_b16 v[228:229], v131 offset:8192
	ds_read_b64_tr_b16 v[230:231], v131 offset:12288
	s_waitcnt lgkmcnt(12)
	v_mfma_f32_16x16x32_bf16 v[136:139], v[200:203], v[34:37], v[136:139]
	ds_read_b64_tr_b16 v[196:197], v124 offset:16384
	ds_read_b64_tr_b16 v[198:199], v124 offset:20480
	s_waitcnt lgkmcnt(12)
	v_mfma_f32_16x16x32_bf16 v[152:155], v[204:207], v[34:37], v[152:155]
	ds_read_b64_tr_b16 v[200:201], v125 offset:16384
	ds_read_b64_tr_b16 v[202:203], v125 offset:20480
	s_waitcnt lgkmcnt(12)
	v_mfma_f32_16x16x32_bf16 v[168:171], v[208:211], v[34:37], v[168:171]
	ds_read_b64_tr_b16 v[204:205], v126 offset:16384
	ds_read_b64_tr_b16 v[206:207], v126 offset:20480
	s_waitcnt lgkmcnt(12)
	v_mfma_f32_16x16x32_bf16 v[172:175], v[212:215], v[34:37], v[172:175]
	ds_read_b64_tr_b16 v[208:209], v127 offset:16384
	ds_read_b64_tr_b16 v[210:211], v127 offset:20480
	s_waitcnt lgkmcnt(12)
	v_mfma_f32_16x16x32_bf16 v[176:179], v[216:219], v[34:37], v[176:179]
	ds_read_b64_tr_b16 v[212:213], v128 offset:16384
	ds_read_b64_tr_b16 v[214:215], v128 offset:20480
	s_waitcnt lgkmcnt(12)
	v_mfma_f32_16x16x32_bf16 v[180:183], v[220:223], v[34:37], v[180:183]
	ds_read_b64_tr_b16 v[216:217], v129 offset:16384
	ds_read_b64_tr_b16 v[218:219], v129 offset:20480
	s_waitcnt lgkmcnt(12)
	v_mfma_f32_16x16x32_bf16 v[192:195], v[228:231], v[34:37], v[192:195]
	ds_read_b64_tr_b16 v[220:221], v130 offset:16384
	ds_read_b64_tr_b16 v[222:223], v130 offset:20480
	s_waitcnt lgkmcnt(12)
	v_mfma_f32_16x16x32_bf16 v[132:135], v[196:199], v[26:29], v[132:135]
	ds_read_b64_tr_b16 v[228:229], v131 offset:16384
	ds_read_b64_tr_b16 v[230:231], v131 offset:20480
	s_waitcnt lgkmcnt(12)
	v_mfma_f32_16x16x32_bf16 v[136:139], v[200:203], v[26:29], v[136:139]
	ds_read_b64_tr_b16 v[196:197], v124 offset:24576
	ds_read_b64_tr_b16 v[198:199], v124 offset:28672
	s_waitcnt lgkmcnt(12)
	v_mfma_f32_16x16x32_bf16 v[152:155], v[204:207], v[26:29], v[152:155]
	ds_read_b64_tr_b16 v[200:201], v125 offset:24576
	ds_read_b64_tr_b16 v[202:203], v125 offset:28672
	s_waitcnt lgkmcnt(12)
	v_mfma_f32_16x16x32_bf16 v[168:171], v[208:211], v[26:29], v[168:171]
	ds_read_b64_tr_b16 v[204:205], v126 offset:24576
	ds_read_b64_tr_b16 v[206:207], v126 offset:28672
	s_waitcnt lgkmcnt(12)
	v_mfma_f32_16x16x32_bf16 v[172:175], v[212:215], v[26:29], v[172:175]
	ds_read_b64_tr_b16 v[208:209], v127 offset:24576
	ds_read_b64_tr_b16 v[210:211], v127 offset:28672
	s_waitcnt lgkmcnt(12)
	v_mfma_f32_16x16x32_bf16 v[176:179], v[216:219], v[26:29], v[176:179]
	ds_read_b64_tr_b16 v[212:213], v128 offset:24576
	ds_read_b64_tr_b16 v[214:215], v128 offset:28672
	s_waitcnt lgkmcnt(12)
	v_mfma_f32_16x16x32_bf16 v[180:183], v[220:223], v[26:29], v[180:183]
	ds_read_b64_tr_b16 v[216:217], v129 offset:24576
	ds_read_b64_tr_b16 v[218:219], v129 offset:28672
	s_waitcnt lgkmcnt(12)
	v_mfma_f32_16x16x32_bf16 v[192:195], v[228:231], v[26:29], v[192:195]
	ds_read_b64_tr_b16 v[220:221], v130 offset:24576
	ds_read_b64_tr_b16 v[222:223], v130 offset:28672
	s_waitcnt lgkmcnt(12)
	v_mfma_f32_16x16x32_bf16 v[132:135], v[196:199], v[10:13], v[132:135]
	ds_read_b64_tr_b16 v[228:229], v131 offset:24576
	ds_read_b64_tr_b16 v[230:231], v131 offset:28672
	s_waitcnt lgkmcnt(12)
	v_mfma_f32_16x16x32_bf16 v[136:139], v[200:203], v[10:13], v[136:139]
	ds_read_b64_tr_b16 v[196:197], v124 offset:32768
	v_mov_b32_e32 v198, v51
	v_mov_b32_e32 v199, v51
	s_waitcnt lgkmcnt(11)
	v_mfma_f32_16x16x32_bf16 v[152:155], v[204:207], v[10:13], v[152:155]
	ds_read_b64_tr_b16 v[200:201], v125 offset:32768
	v_mov_b32_e32 v202, v51
	v_mov_b32_e32 v203, v51
	s_waitcnt lgkmcnt(10)
	v_mfma_f32_16x16x32_bf16 v[168:171], v[208:211], v[10:13], v[168:171]
	ds_read_b64_tr_b16 v[204:205], v126 offset:32768
	v_mov_b32_e32 v206, v51
	v_mov_b32_e32 v207, v51
	s_waitcnt lgkmcnt(9)
	v_mfma_f32_16x16x32_bf16 v[172:175], v[212:215], v[10:13], v[172:175]
	ds_read_b64_tr_b16 v[208:209], v127 offset:32768
	v_mov_b32_e32 v210, v51
	v_mov_b32_e32 v211, v51
	s_waitcnt lgkmcnt(8)
	v_mfma_f32_16x16x32_bf16 v[176:179], v[216:219], v[10:13], v[176:179]
	ds_read_b64_tr_b16 v[212:213], v128 offset:32768
	v_mov_b32_e32 v214, v51
	v_mov_b32_e32 v215, v51
	s_waitcnt lgkmcnt(7)
	v_mfma_f32_16x16x32_bf16 v[180:183], v[220:223], v[10:13], v[180:183]
	ds_read_b64_tr_b16 v[216:217], v129 offset:32768
	v_mov_b32_e32 v218, v51
	v_mov_b32_e32 v219, v51
	s_waitcnt lgkmcnt(6)
	v_mfma_f32_16x16x32_bf16 v[192:195], v[228:231], v[10:13], v[192:195]
	ds_read_b64_tr_b16 v[220:221], v130 offset:32768
	v_mov_b32_e32 v222, v51
	v_mov_b32_e32 v223, v51
	s_waitcnt lgkmcnt(6)
	v_mfma_f32_16x16x32_bf16 v[14:17], v[196:199], v[6:9], v[132:135]
	ds_read_b64_tr_b16 v[228:229], v131 offset:32768
	v_mov_b32_e32 v230, v51
	v_mov_b32_e32 v231, v51
	s_waitcnt lgkmcnt(6)
	v_mfma_f32_16x16x32_bf16 v[26:29], v[200:203], v[6:9], v[136:139]
	s_waitcnt lgkmcnt(5)
	v_mfma_f32_16x16x32_bf16 v[30:33], v[204:207], v[6:9], v[152:155]
	s_waitcnt lgkmcnt(4)
	v_mfma_f32_16x16x32_bf16 v[34:37], v[208:211], v[6:9], v[168:171]
	s_waitcnt lgkmcnt(3)
	v_mfma_f32_16x16x32_bf16 v[18:21], v[212:215], v[6:9], v[172:175]
	s_waitcnt lgkmcnt(2)
	v_mfma_f32_16x16x32_bf16 v[38:41], v[216:219], v[6:9], v[176:179]
	s_waitcnt lgkmcnt(1)
	v_mfma_f32_16x16x32_bf16 v[42:45], v[220:223], v[6:9], v[180:183]
	s_waitcnt lgkmcnt(0)
	v_mfma_f32_16x16x32_bf16 v[6:9], v[228:231], v[6:9], v[192:195]
	s_nop 2
	v_fma_f32 v10, -v4, v5, 1.0
	v_fmac_f32_e32 v5, v10, v5
	v_div_scale_f32 v10, vcc, 1.0, v2, 1.0
	v_mul_f32_e32 v11, v10, v5
	v_fma_f32 v12, -v4, v11, v10
	v_fmac_f32_e32 v11, v12, v5
	v_fma_f32 v4, -v4, v11, v10
	v_div_fmas_f32 v4, v4, v5, v11
	v_div_fixup_f32 v22, v4, v2, 1.0
	v_lshlrev_b64 v[4:5], s59, v[50:51]
	s_ashr_i32 s59, s58, 31
	s_lshl_b64 s[58:59], s[58:59], 14
	s_add_u32 s58, s58, s64
	s_addc_u32 s59, s59, s65
	s_or_b32 s58, s58, s57
	v_lshl_add_u64 v[4:5], s[58:59], 0, v[4:5]
	v_mov_b64_e32 v[10:11], s[22:23]
	v_mad_u64_u32 v[10:11], s[58:59], v4, s45, v[10:11]
	v_mad_i32_i24 v11, v5, s45, v11
	v_mul_f32_e32 v12, v22, v14
	v_mul_f32_e32 v13, v22, v15
	v_lshl_add_u64 v[10:11], v[10:11], 0, s[66:67]
	v_cvt_pk_bf16_f32 v12, v12, v13
	v_mul_f32_e32 v13, v22, v16
	v_lshl_add_u64 v[10:11], v[10:11], 0, v[56:57]
	v_mul_f32_e32 v14, v22, v17
	v_cvt_pk_bf16_f32 v13, v13, v14
	global_store_dwordx2 v[10:11], v[12:13], off
	v_mul_f32_e32 v12, v22, v26
	v_mul_f32_e32 v13, v22, v27
	v_cvt_pk_bf16_f32 v12, v12, v13
	v_mul_f32_e32 v13, v22, v28
	v_mul_f32_e32 v14, v22, v29
	v_cvt_pk_bf16_f32 v13, v13, v14
	global_store_dwordx2 v[10:11], v[12:13], off offset:32
	v_mul_f32_e32 v12, v22, v30
	v_mul_f32_e32 v13, v22, v31
	v_cvt_pk_bf16_f32 v12, v12, v13
	v_mul_f32_e32 v13, v22, v32
	v_mul_f32_e32 v14, v22, v33
	v_cvt_pk_bf16_f32 v13, v13, v14
	global_store_dwordx2 v[10:11], v[12:13], off offset:64
	v_mul_f32_e32 v12, v22, v34
	v_mul_f32_e32 v13, v22, v35
	v_cvt_pk_bf16_f32 v12, v12, v13
	v_mul_f32_e32 v13, v22, v36
	v_mul_f32_e32 v14, v22, v37
	v_cvt_pk_bf16_f32 v13, v13, v14
	global_store_dwordx2 v[10:11], v[12:13], off offset:96
	v_mul_f32_e32 v12, v22, v18
	v_mul_f32_e32 v13, v22, v19
	v_cvt_pk_bf16_f32 v12, v12, v13
	v_mul_f32_e32 v13, v22, v20
	v_mul_f32_e32 v14, v22, v21
	v_cvt_pk_bf16_f32 v13, v13, v14
	global_store_dwordx2 v[10:11], v[12:13], off offset:128
	v_mul_f32_e32 v12, v22, v38
	v_mul_f32_e32 v13, v22, v39
	v_cvt_pk_bf16_f32 v12, v12, v13
	v_mul_f32_e32 v13, v22, v40
	v_mul_f32_e32 v14, v22, v41
	v_cvt_pk_bf16_f32 v13, v13, v14
	global_store_dwordx2 v[10:11], v[12:13], off offset:160
	v_mul_f32_e32 v12, v22, v42
	v_mul_f32_e32 v13, v22, v43
	v_cvt_pk_bf16_f32 v12, v12, v13
	v_mul_f32_e32 v13, v22, v44
	v_mul_f32_e32 v6, v22, v6
	v_mul_f32_e32 v7, v22, v7
	v_mul_f32_e32 v14, v22, v45
	v_cvt_pk_bf16_f32 v13, v13, v14
	global_store_dwordx2 v[10:11], v[12:13], off offset:192
	v_cvt_pk_bf16_f32 v6, v6, v7
	v_mul_f32_e32 v7, v22, v8
	v_mul_f32_e32 v8, v22, v9
	v_cvt_pk_bf16_f32 v7, v7, v8
	global_store_dwordx2 v[10:11], v[6:7], off offset:224
	s_and_saveexec_b64 s[58:59], s[4:5]
	s_cbranch_execz .LBB0_242
	s_mov_b32 s57, 0x800000
	v_cmp_gt_f32_e32 vcc, s57, v2
	s_mov_b32 s57, 0x3f317217
	s_nop 0
	v_cndmask_b32_e64 v6, 0, 32, vcc
	v_ldexp_f32 v2, v2, v6
	v_log_f32_e32 v2, v2
	v_cndmask_b32_e32 v6, 0, v102, vcc
	v_mul_f32_e32 v7, 0x3f317217, v2
	v_fma_f32 v7, v2, s57, -v7
	v_fmac_f32_e32 v7, 0x3377d1cf, v2
	s_mov_b32 s57, 0x7f800000
	v_fmac_f32_e32 v7, 0x3f317217, v2
	v_cmp_lt_f32_e64 vcc, |v2|, s57
	s_ashr_i32 s57, s56, 31
	s_nop 0
	v_cndmask_b32_e32 v2, v2, v7, vcc
	v_sub_f32_e32 v6, v2, v6
	v_fmac_f32_e32 v6, 0x3db504f3, v3
	v_mad_u64_u32 v[2:3], s[60:61], v4, 48, s[24:25]
	v_mov_b32_e32 v4, v3
	v_mad_u64_u32 v[4:5], s[60:61], v5, 48, v[4:5]
	v_mov_b32_e32 v3, v4
	v_lshl_add_u64 v[2:3], s[56:57], 2, v[2:3]
	global_store_dword v[2:3], v6, off
	s_branch .LBB0_242
